# prep phase: the 36 serially waited loads of the k/v projection tile issued together (counted vmcnt), on top of the relu cleanup
# speedup vs baseline: 1.0028x; 1.0028x over previous
.LBB0_466:
	v_mov_b64_e32 v[0:1], s[4:5]
	v_mad_i64_i32 v[0:1], s[18:19], v86, s10, v[0:1]
	v_mov_b32_e32 v89, v48
	v_lshl_add_u64 v[0:1], v[0:1], 0, v[88:89]
	s_mov_b64 s[18:19], 0x1400
	v_lshl_add_u64 v[12:13], v[0:1], 0, s[18:19]
	v_add_co_u32_e32 v0, vcc, 0x1000, v0
	v_ashrrev_i32_e32 v87, 31, v86
	s_nop 0
	v_addc_co_u32_e32 v1, vcc, 0, v1, vcc
	global_load_dwordx4 v[0:3], v[0:1], off offset:1024
	global_load_dwordx4 v[220:223], v[12:13], off offset:64
	global_load_dwordx4 v[224:227], v[12:13], off offset:128
	global_load_dwordx4 v[228:231], v[12:13], off offset:192
	global_load_dwordx4 v[108:111], v[26:27], off offset:64
	global_load_dwordx4 v[112:115], v[26:27], off
	global_load_dwordx4 v[116:119], v[26:27], off offset:128
	global_load_dwordx4 v[120:123], v[26:27], off offset:192
	global_load_dwordx4 v[124:127], v[28:29], off
	global_load_dwordx4 v[128:131], v[30:31], off
	global_load_dwordx4 v[132:135], v[32:33], off
	global_load_dwordx4 v[136:139], v[34:35], off
	global_load_dwordx4 v[140:143], v[36:37], off
	global_load_dwordx4 v[144:147], v[38:39], off
	global_load_dwordx4 v[148:151], v[40:41], off
	global_load_dwordx4 v[152:155], v[42:43], off
	global_load_dwordx4 v[156:159], v[44:45], off
	global_load_dwordx4 v[160:163], v[46:47], off
	global_load_dwordx4 v[164:167], v[50:51], off
	global_load_dwordx4 v[168:171], v[52:53], off
	global_load_dwordx4 v[172:175], v[54:55], off
	global_load_dwordx4 v[176:179], v[56:57], off
	global_load_dwordx4 v[180:183], v[58:59], off
	global_load_dwordx4 v[184:187], v[60:61], off
	global_load_dwordx4 v[188:191], v[62:63], off
	global_load_dwordx4 v[192:195], v[64:65], off
	global_load_dwordx4 v[196:199], v[66:67], off
	global_load_dwordx4 v[200:203], v[68:69], off
	global_load_dwordx4 v[204:207], v[70:71], off
	global_load_dwordx4 v[208:211], v[72:73], off
	global_load_dwordx4 v[212:215], v[74:75], off
	global_load_dwordx4 v[216:219], v[76:77], off
	s_add_i32 s1, s1, s7
	s_cmp_lt_i32 s1, s8
	s_waitcnt vmcnt(31)
	v_and_b32_e32 v5, 0xffff0000, v1
	v_lshlrev_b32_e32 v4, 16, v1
	v_mul_f32_e32 v6, v5, v5
	v_and_b32_e32 v9, 0xffff0000, v0
	v_and_b32_e32 v8, 0xffff0000, v2
	v_pk_fma_f32 v[4:5], v[4:5], v[4:5], v[6:7] op_sel_hi:[1,1,0]
	v_lshlrev_b32_e32 v7, 16, v0
	v_lshlrev_b32_e32 v6, 16, v2
	v_pk_mul_f32 v[8:9], v[8:9], v[8:9]
	v_and_b32_e32 v19, 0xffff0000, v3
	v_pk_fma_f32 v[6:7], v[6:7], v[6:7], v[8:9]
	v_lshlrev_b32_e32 v18, 16, v3
	v_pk_add_f32 v[4:5], v[6:7], v[4:5] op_sel:[1,0] op_sel_hi:[0,1]
	v_pk_add_f32 v[16:17], v[6:7], v[4:5]
	s_waitcnt vmcnt(30)
	v_mov_b32_e32 v4, v220
	v_mov_b32_e32 v5, v221
	v_mov_b32_e32 v6, v222
	v_mov_b32_e32 v7, v223
	v_and_b32_e32 v11, 0xffff0000, v5
	v_and_b32_e32 v10, 0xffff0000, v4
	v_lshlrev_b32_e32 v9, 16, v5
	v_lshlrev_b32_e32 v8, 16, v4
	v_pk_mul_f32 v[10:11], v[10:11], v[10:11]
	v_and_b32_e32 v15, 0xffff0000, v7
	v_and_b32_e32 v14, 0xffff0000, v6
	v_pk_fma_f32 v[8:9], v[8:9], v[8:9], v[10:11]
	v_lshlrev_b32_e32 v11, 16, v7
	v_lshlrev_b32_e32 v10, 16, v6
	v_pk_mul_f32 v[14:15], v[14:15], v[14:15]
	v_pk_add_f32 v[8:9], v[8:9], v[8:9] op_sel:[0,1] op_sel_hi:[1,0]
	v_pk_fma_f32 v[20:21], v[10:11], v[10:11], v[14:15]
	s_nop 0
	v_pk_add_f32 v[22:23], v[20:21], v[8:9]
	s_waitcnt vmcnt(29)
	v_mov_b32_e32 v8, v224
	v_mov_b32_e32 v9, v225
	v_mov_b32_e32 v10, v226
	v_mov_b32_e32 v11, v227
	v_and_b32_e32 v91, 0xffff0000, v8
	v_lshlrev_b32_e32 v90, 16, v8
	v_and_b32_e32 v95, 0xffff0000, v9
	v_lshlrev_b32_e32 v94, 16, v9
	v_and_b32_e32 v100, 0xffff0000, v10
	v_lshlrev_b32_e32 v98, 16, v10
	v_lshlrev_b32_e32 v104, 16, v11
	s_waitcnt vmcnt(28)
	v_mov_b32_e32 v12, v228
	v_mov_b32_e32 v13, v229
	v_mov_b32_e32 v14, v230
	v_mov_b32_e32 v15, v231
	v_and_b32_e32 v92, 0xffff0000, v13
	v_mul_f32_e32 v106, v92, v92
	v_mul_f32_e32 v92, v91, v91
	v_lshlrev_b32_e32 v89, 16, v13
	v_pk_fma_f32 v[90:91], v[90:91], v[90:91], v[92:93] op_sel_hi:[1,1,0]
	v_mul_f32_e32 v92, v95, v95
	v_mul_f32_e32 v89, v89, v89
	v_and_b32_e32 v101, 0xffff0000, v12
	v_pk_mov_b32 v[102:103], v[10:11], v[14:15] op_sel:[1,0]
	v_pk_fma_f32 v[94:95], v[94:95], v[94:95], v[92:93] op_sel_hi:[1,1,0]
	v_lshlrev_b32_e32 v99, 16, v12
	v_and_b32_e32 v103, 0xffff0000, v103
	v_and_b32_e32 v102, 0xffff0000, v102
	v_pk_mul_f32 v[100:101], v[100:101], v[100:101]
	v_mov_b32_e32 v91, v89
	v_mov_b32_e32 v95, v106
	v_lshlrev_b32_e32 v105, 16, v14
	v_pk_fma_f32 v[98:99], v[98:99], v[98:99], v[100:101]
	v_pk_add_f32 v[90:91], v[90:91], v[94:95]
	v_pk_mul_f32 v[94:95], v[102:103], v[102:103]
	v_mul_f32_e32 v92, v19, v19
	v_lshlrev_b32_e32 v97, 16, v15
	v_and_b32_e32 v96, 0xffff0000, v15
	v_pk_add_f32 v[90:91], v[98:99], v[90:91]
	v_pk_fma_f32 v[94:95], v[104:105], v[104:105], v[94:95]
	v_pk_fma_f32 v[18:19], v[18:19], v[18:19], v[92:93] op_sel_hi:[1,1,0]
	v_mul_f32_e32 v107, v96, v96
	v_pk_add_f32 v[90:91], v[94:95], v[90:91]
	v_mov_b32_e32 v96, v18
	v_mov_b32_e32 v94, v16
	v_mov_b32_e32 v95, v97
	v_pk_add_f32 v[16:17], v[18:19], v[16:17]
	v_pk_mul_f32 v[18:19], v[96:97], v[94:95]
	s_nop 0
	v_mov_b32_e32 v17, v19
	v_pk_add_f32 v[18:19], v[20:21], v[22:23] op_sel:[1,0] op_sel_hi:[0,1]
	v_mov_b32_e32 v19, v107
	v_pk_add_f32 v[16:17], v[16:17], v[18:19]
	v_pk_add_f32 v[16:17], v[16:17], v[90:91]
	s_nop 0
	v_add_f32_e32 v16, v16, v17
	ds_bpermute_b32 v17, v49, v16
	s_waitcnt lgkmcnt(0)
	v_add_f32_e32 v16, v16, v17
	ds_bpermute_b32 v17, v93, v16
	s_waitcnt lgkmcnt(0)
	v_add_f32_e32 v16, v16, v17
	v_fmamk_f32 v16, v16, 0x3c000000, v237
	v_cmp_gt_f32_e32 vcc, s13, v16
	v_mul_f32_e32 v17, 0x4b800000, v16
	s_nop 0
	v_cndmask_b32_e32 v16, v16, v17, vcc
	v_rsq_f32_e32 v16, v16
	s_nop 0
	v_mul_f32_e32 v17, 0x45800000, v16
	v_cndmask_b32_e32 v92, v16, v17, vcc
	v_lshlrev_b64 v[16:17], 8, v[86:87]
	v_lshl_add_u64 v[90:91], v[24:25], 0, v[16:17]
	s_waitcnt vmcnt(0)
	v_mfma_f32_16x16x32_bf16 v[16:19], v[112:115], v[0:3], 0
	v_add_u32_e32 v86, s6, v86
	v_mfma_f32_16x16x32_bf16 v[16:19], v[108:111], v[4:7], v[16:19]
	v_mfma_f32_16x16x32_bf16 v[16:19], v[116:119], v[8:11], v[16:19]
	v_mfma_f32_16x16x32_bf16 v[16:19], v[120:123], v[12:15], v[16:19]
	global_load_dwordx4 v[108:111], v[78:79], off
	global_load_dwordx4 v[112:115], v[80:81], off
	global_load_dwordx4 v[116:119], v[82:83], off
	global_load_dwordx4 v[120:123], v[84:85], off
	s_nop 7
	v_mov_b32_e32 v20, v16
	v_mov_b32_e32 v21, v18
	v_pk_mul_f32 v[20:21], v[20:21], v[92:93] op_sel_hi:[1,0]
	v_mov_b32_e32 v18, v17
	v_pk_mul_f32 v[16:17], v[18:19], v[92:93] op_sel_hi:[1,0]
	v_and_b32_sdwa v18, v21, v236 dst_sel:DWORD dst_unused:UNUSED_PAD src0_sel:WORD_1 src1_sel:DWORD
	v_and_b32_sdwa v19, v20, v236 dst_sel:DWORD dst_unused:UNUSED_PAD src0_sel:WORD_1 src1_sel:DWORD
	v_add3_u32 v19, v20, v19, s75
	v_add3_u32 v18, v21, v18, s75
	v_and_b32_sdwa v20, v17, v236 dst_sel:DWORD dst_unused:UNUSED_PAD src0_sel:WORD_1 src1_sel:DWORD
	v_and_b32_sdwa v21, v16, v236 dst_sel:DWORD dst_unused:UNUSED_PAD src0_sel:WORD_1 src1_sel:DWORD
	v_add3_u32 v17, v17, v20, s75
	v_add3_u32 v16, v16, v21, s75
	v_and_b32_e32 v17, 0xffff0000, v17
	v_and_b32_e32 v16, 0xffff0000, v16
	v_or_b32_sdwa v17, v17, v18 dst_sel:DWORD dst_unused:UNUSED_PAD src0_sel:DWORD src1_sel:WORD_1
	v_or_b32_sdwa v16, v16, v19 dst_sel:DWORD dst_unused:UNUSED_PAD src0_sel:DWORD src1_sel:WORD_1
	global_store_dwordx2 v[90:91], v[16:17], off
	s_nop 0
	v_mfma_f32_16x16x32_bf16 v[16:19], v[124:127], v[0:3], 0
	v_mfma_f32_16x16x32_bf16 v[16:19], v[128:131], v[4:7], v[16:19]
	v_mfma_f32_16x16x32_bf16 v[16:19], v[132:135], v[8:11], v[16:19]
	v_mfma_f32_16x16x32_bf16 v[16:19], v[136:139], v[12:15], v[16:19]
	s_nop 7
	v_mov_b32_e32 v20, v16
	v_mov_b32_e32 v21, v18
	v_pk_mul_f32 v[20:21], v[92:93], v[20:21] op_sel_hi:[0,1]
	v_mov_b32_e32 v18, v17
	v_pk_mul_f32 v[16:17], v[92:93], v[18:19] op_sel_hi:[0,1]
	v_and_b32_sdwa v18, v21, v236 dst_sel:DWORD dst_unused:UNUSED_PAD src0_sel:WORD_1 src1_sel:DWORD
	v_and_b32_sdwa v19, v20, v236 dst_sel:DWORD dst_unused:UNUSED_PAD src0_sel:WORD_1 src1_sel:DWORD
	v_add3_u32 v19, v20, v19, s75
	v_add3_u32 v18, v21, v18, s75
	v_and_b32_sdwa v20, v17, v236 dst_sel:DWORD dst_unused:UNUSED_PAD src0_sel:WORD_1 src1_sel:DWORD
	v_and_b32_sdwa v21, v16, v236 dst_sel:DWORD dst_unused:UNUSED_PAD src0_sel:WORD_1 src1_sel:DWORD
	v_add3_u32 v17, v17, v20, s75
	v_add3_u32 v16, v16, v21, s75
	v_and_b32_e32 v17, 0xffff0000, v17
	v_and_b32_e32 v16, 0xffff0000, v16
	v_or_b32_sdwa v17, v17, v18 dst_sel:DWORD dst_unused:UNUSED_PAD src0_sel:DWORD src1_sel:WORD_1
	v_or_b32_sdwa v16, v16, v19 dst_sel:DWORD dst_unused:UNUSED_PAD src0_sel:DWORD src1_sel:WORD_1
	global_store_dwordx2 v[90:91], v[16:17], off offset:32
	s_nop 0
	v_mfma_f32_16x16x32_bf16 v[16:19], v[140:143], v[0:3], 0
	v_mfma_f32_16x16x32_bf16 v[16:19], v[144:147], v[4:7], v[16:19]
	v_mfma_f32_16x16x32_bf16 v[16:19], v[148:151], v[8:11], v[16:19]
	v_mfma_f32_16x16x32_bf16 v[16:19], v[152:155], v[12:15], v[16:19]
	s_nop 7
	v_mov_b32_e32 v20, v16
	v_mov_b32_e32 v21, v18
	v_pk_mul_f32 v[20:21], v[92:93], v[20:21] op_sel_hi:[0,1]
	v_mov_b32_e32 v18, v17
	v_pk_mul_f32 v[16:17], v[92:93], v[18:19] op_sel_hi:[0,1]
	v_and_b32_sdwa v18, v21, v236 dst_sel:DWORD dst_unused:UNUSED_PAD src0_sel:WORD_1 src1_sel:DWORD
	v_and_b32_sdwa v19, v20, v236 dst_sel:DWORD dst_unused:UNUSED_PAD src0_sel:WORD_1 src1_sel:DWORD
	v_add3_u32 v19, v20, v19, s75
	v_add3_u32 v18, v21, v18, s75
	v_and_b32_sdwa v20, v17, v236 dst_sel:DWORD dst_unused:UNUSED_PAD src0_sel:WORD_1 src1_sel:DWORD
	v_and_b32_sdwa v21, v16, v236 dst_sel:DWORD dst_unused:UNUSED_PAD src0_sel:WORD_1 src1_sel:DWORD
	v_add3_u32 v17, v17, v20, s75
	v_add3_u32 v16, v16, v21, s75
	v_and_b32_e32 v17, 0xffff0000, v17
	v_and_b32_e32 v16, 0xffff0000, v16
	v_or_b32_sdwa v17, v17, v18 dst_sel:DWORD dst_unused:UNUSED_PAD src0_sel:DWORD src1_sel:WORD_1
	v_or_b32_sdwa v16, v16, v19 dst_sel:DWORD dst_unused:UNUSED_PAD src0_sel:DWORD src1_sel:WORD_1
	global_store_dwordx2 v[90:91], v[16:17], off offset:64
	s_nop 0
	v_mfma_f32_16x16x32_bf16 v[16:19], v[156:159], v[0:3], 0
	v_mfma_f32_16x16x32_bf16 v[16:19], v[160:163], v[4:7], v[16:19]
	v_mfma_f32_16x16x32_bf16 v[16:19], v[164:167], v[8:11], v[16:19]
	v_mfma_f32_16x16x32_bf16 v[16:19], v[168:171], v[12:15], v[16:19]
	s_nop 7
	v_mov_b32_e32 v20, v16
	v_mov_b32_e32 v21, v18
	v_pk_mul_f32 v[20:21], v[92:93], v[20:21] op_sel_hi:[0,1]
	v_mov_b32_e32 v18, v17
	v_pk_mul_f32 v[16:17], v[92:93], v[18:19] op_sel_hi:[0,1]
	v_and_b32_sdwa v18, v21, v236 dst_sel:DWORD dst_unused:UNUSED_PAD src0_sel:WORD_1 src1_sel:DWORD
	v_and_b32_sdwa v19, v20, v236 dst_sel:DWORD dst_unused:UNUSED_PAD src0_sel:WORD_1 src1_sel:DWORD
	v_add3_u32 v19, v20, v19, s75
	v_add3_u32 v18, v21, v18, s75
	v_and_b32_sdwa v20, v17, v236 dst_sel:DWORD dst_unused:UNUSED_PAD src0_sel:WORD_1 src1_sel:DWORD
	v_and_b32_sdwa v21, v16, v236 dst_sel:DWORD dst_unused:UNUSED_PAD src0_sel:WORD_1 src1_sel:DWORD
	v_add3_u32 v17, v17, v20, s75
	v_add3_u32 v16, v16, v21, s75
	v_and_b32_e32 v17, 0xffff0000, v17
	v_and_b32_e32 v16, 0xffff0000, v16
	v_or_b32_sdwa v17, v17, v18 dst_sel:DWORD dst_unused:UNUSED_PAD src0_sel:DWORD src1_sel:WORD_1
	v_or_b32_sdwa v16, v16, v19 dst_sel:DWORD dst_unused:UNUSED_PAD src0_sel:DWORD src1_sel:WORD_1
	global_store_dwordx2 v[90:91], v[16:17], off offset:96
	s_nop 0
	v_mfma_f32_16x16x32_bf16 v[16:19], v[172:175], v[0:3], 0
	v_mfma_f32_16x16x32_bf16 v[16:19], v[176:179], v[4:7], v[16:19]
	v_mfma_f32_16x16x32_bf16 v[16:19], v[180:183], v[8:11], v[16:19]
	v_mfma_f32_16x16x32_bf16 v[16:19], v[184:187], v[12:15], v[16:19]
	s_nop 7
	v_mov_b32_e32 v20, v16
	v_mov_b32_e32 v21, v18
	v_pk_mul_f32 v[20:21], v[92:93], v[20:21] op_sel_hi:[0,1]
	v_mov_b32_e32 v18, v17
	v_pk_mul_f32 v[16:17], v[92:93], v[18:19] op_sel_hi:[0,1]
	v_and_b32_sdwa v18, v21, v236 dst_sel:DWORD dst_unused:UNUSED_PAD src0_sel:WORD_1 src1_sel:DWORD
	v_and_b32_sdwa v19, v20, v236 dst_sel:DWORD dst_unused:UNUSED_PAD src0_sel:WORD_1 src1_sel:DWORD
	v_add3_u32 v19, v20, v19, s75
	v_add3_u32 v18, v21, v18, s75
	v_and_b32_sdwa v20, v17, v236 dst_sel:DWORD dst_unused:UNUSED_PAD src0_sel:WORD_1 src1_sel:DWORD
	v_and_b32_sdwa v21, v16, v236 dst_sel:DWORD dst_unused:UNUSED_PAD src0_sel:WORD_1 src1_sel:DWORD
	v_add3_u32 v17, v17, v20, s75
	v_add3_u32 v16, v16, v21, s75
	v_and_b32_e32 v17, 0xffff0000, v17
	v_and_b32_e32 v16, 0xffff0000, v16
	v_or_b32_sdwa v17, v17, v18 dst_sel:DWORD dst_unused:UNUSED_PAD src0_sel:DWORD src1_sel:WORD_1
	v_or_b32_sdwa v16, v16, v19 dst_sel:DWORD dst_unused:UNUSED_PAD src0_sel:DWORD src1_sel:WORD_1
	global_store_dwordx2 v[90:91], v[16:17], off offset:128
	s_nop 0
	v_mfma_f32_16x16x32_bf16 v[16:19], v[188:191], v[0:3], 0
	v_mfma_f32_16x16x32_bf16 v[16:19], v[192:195], v[4:7], v[16:19]
	v_mfma_f32_16x16x32_bf16 v[16:19], v[196:199], v[8:11], v[16:19]
	v_mfma_f32_16x16x32_bf16 v[16:19], v[200:203], v[12:15], v[16:19]
	s_nop 7
	v_mov_b32_e32 v20, v16
	v_mov_b32_e32 v21, v18
	v_pk_mul_f32 v[20:21], v[92:93], v[20:21] op_sel_hi:[0,1]
	v_mov_b32_e32 v18, v17
	v_pk_mul_f32 v[16:17], v[92:93], v[18:19] op_sel_hi:[0,1]
	v_and_b32_sdwa v18, v21, v236 dst_sel:DWORD dst_unused:UNUSED_PAD src0_sel:WORD_1 src1_sel:DWORD
	v_and_b32_sdwa v19, v20, v236 dst_sel:DWORD dst_unused:UNUSED_PAD src0_sel:WORD_1 src1_sel:DWORD
	v_add3_u32 v19, v20, v19, s75
	v_add3_u32 v18, v21, v18, s75
	v_and_b32_sdwa v20, v17, v236 dst_sel:DWORD dst_unused:UNUSED_PAD src0_sel:WORD_1 src1_sel:DWORD
	v_and_b32_sdwa v21, v16, v236 dst_sel:DWORD dst_unused:UNUSED_PAD src0_sel:WORD_1 src1_sel:DWORD
	v_add3_u32 v17, v17, v20, s75
	v_add3_u32 v16, v16, v21, s75
	v_and_b32_e32 v17, 0xffff0000, v17
	v_and_b32_e32 v16, 0xffff0000, v16
	v_or_b32_sdwa v17, v17, v18 dst_sel:DWORD dst_unused:UNUSED_PAD src0_sel:DWORD src1_sel:WORD_1
	v_or_b32_sdwa v16, v16, v19 dst_sel:DWORD dst_unused:UNUSED_PAD src0_sel:DWORD src1_sel:WORD_1
	global_store_dwordx2 v[90:91], v[16:17], off offset:160
	s_nop 0
	v_mfma_f32_16x16x32_bf16 v[16:19], v[204:207], v[0:3], 0
	v_mfma_f32_16x16x32_bf16 v[16:19], v[208:211], v[4:7], v[16:19]
	v_mfma_f32_16x16x32_bf16 v[16:19], v[212:215], v[8:11], v[16:19]
	v_mfma_f32_16x16x32_bf16 v[16:19], v[216:219], v[12:15], v[16:19]
	s_nop 7
	v_mov_b32_e32 v20, v16
	v_mov_b32_e32 v21, v18
	v_pk_mul_f32 v[20:21], v[92:93], v[20:21] op_sel_hi:[0,1]
	v_mov_b32_e32 v18, v17
	v_pk_mul_f32 v[16:17], v[92:93], v[18:19] op_sel_hi:[0,1]
	v_and_b32_sdwa v18, v21, v236 dst_sel:DWORD dst_unused:UNUSED_PAD src0_sel:WORD_1 src1_sel:DWORD
	v_and_b32_sdwa v19, v20, v236 dst_sel:DWORD dst_unused:UNUSED_PAD src0_sel:WORD_1 src1_sel:DWORD
	v_add3_u32 v19, v20, v19, s75
	v_add3_u32 v18, v21, v18, s75
	v_and_b32_sdwa v20, v17, v236 dst_sel:DWORD dst_unused:UNUSED_PAD src0_sel:WORD_1 src1_sel:DWORD
	v_and_b32_sdwa v21, v16, v236 dst_sel:DWORD dst_unused:UNUSED_PAD src0_sel:WORD_1 src1_sel:DWORD
	v_add3_u32 v17, v17, v20, s75
	v_add3_u32 v16, v16, v21, s75
	v_and_b32_e32 v17, 0xffff0000, v17
	v_and_b32_e32 v16, 0xffff0000, v16
	v_or_b32_sdwa v17, v17, v18 dst_sel:DWORD dst_unused:UNUSED_PAD src0_sel:DWORD src1_sel:WORD_1
	v_or_b32_sdwa v16, v16, v19 dst_sel:DWORD dst_unused:UNUSED_PAD src0_sel:DWORD src1_sel:WORD_1
	global_store_dwordx2 v[90:91], v[16:17], off offset:192
	s_waitcnt vmcnt(7)
	v_mfma_f32_16x16x32_bf16 v[0:3], v[108:111], v[0:3], 0
	v_mfma_f32_16x16x32_bf16 v[0:3], v[112:115], v[4:7], v[0:3]
	v_mfma_f32_16x16x32_bf16 v[0:3], v[116:119], v[8:11], v[0:3]
	v_mfma_f32_16x16x32_bf16 v[0:3], v[120:123], v[12:15], v[0:3]
	s_nop 7
	v_mov_b32_e32 v4, v0
	v_mov_b32_e32 v5, v2
	v_pk_mul_f32 v[4:5], v[92:93], v[4:5] op_sel_hi:[0,1]
	v_mov_b32_e32 v2, v1
	v_pk_mul_f32 v[0:1], v[92:93], v[2:3] op_sel_hi:[0,1]
	v_and_b32_sdwa v2, v5, v236 dst_sel:DWORD dst_unused:UNUSED_PAD src0_sel:WORD_1 src1_sel:DWORD
	v_and_b32_sdwa v3, v4, v236 dst_sel:DWORD dst_unused:UNUSED_PAD src0_sel:WORD_1 src1_sel:DWORD
	v_add3_u32 v3, v4, v3, s75
	v_add3_u32 v2, v5, v2, s75
	v_and_b32_sdwa v4, v1, v236 dst_sel:DWORD dst_unused:UNUSED_PAD src0_sel:WORD_1 src1_sel:DWORD
	v_and_b32_sdwa v5, v0, v236 dst_sel:DWORD dst_unused:UNUSED_PAD src0_sel:WORD_1 src1_sel:DWORD
	v_add3_u32 v1, v1, v4, s75
	v_add3_u32 v0, v0, v5, s75
	v_and_b32_e32 v1, 0xffff0000, v1
	v_and_b32_e32 v0, 0xffff0000, v0
	v_or_b32_sdwa v1, v1, v2 dst_sel:DWORD dst_unused:UNUSED_PAD src0_sel:DWORD src1_sel:WORD_1
	v_or_b32_sdwa v0, v0, v3 dst_sel:DWORD dst_unused:UNUSED_PAD src0_sel:DWORD src1_sel:WORD_1
	global_store_dwordx2 v[90:91], v[0:1], off offset:224
	s_cbranch_scc1 .LBB0_466
